# speedup vs baseline: 1.0035x; 1.0035x over previous
.Lsc_dskip15:
	s_waitcnt lgkmcnt(0)
	s_barrier
	v_lshlrev_b32_e32 v50, 3, v0
	v_mov_b32_e32 v52, 0
	v_mov_b32_e32 v53, 0
	v_cmp_gt_u32_e32 vcc, 0x224, v0
	s_and_saveexec_b64 s[36:37], vcc
	ds_read_b64 v[52:53], v50 offset:4608
	s_mov_b64 exec, s[36:37]
	s_waitcnt lgkmcnt(0)
	v_add_u32_e32 v54, v52, v53
	v_mov_b32_e32 v55, v54
	s_nop 1
	v_add_u32_dpp v55, v55, v55 row_shr:1 row_mask:0xf bank_mask:0xf bound_ctrl:0
	s_nop 1
	v_add_u32_dpp v55, v55, v55 row_shr:2 row_mask:0xf bank_mask:0xf bound_ctrl:0
	s_nop 1
	v_add_u32_dpp v55, v55, v55 row_shr:4 row_mask:0xf bank_mask:0xf bound_ctrl:0
	s_nop 1
	v_add_u32_dpp v55, v55, v55 row_shr:8 row_mask:0xf bank_mask:0xf bound_ctrl:0
	s_nop 1
	v_add_u32_dpp v55, v55, v55 row_bcast:15 row_mask:0xa bank_mask:0xf
	s_nop 1
	v_add_u32_dpp v55, v55, v55 row_bcast:31 row_mask:0xc bank_mask:0xf
	v_lshrrev_b32_e32 v56, 6, v0
	s_nop 0
	v_readfirstlane_b32 s3, v56
	v_readlane_b32 s14, v55, 63
	s_lshl_b32 s15, s3, 2
	s_add_u32 s15, s15, 0x2400
	v_mov_b32_e32 v57, s14
	v_mov_b32_e32 v58, s15
	s_mov_b64 s[38:39], exec
	s_mov_b64 exec, 1
	ds_write_b32 v58, v57
	s_mov_b64 exec, s[38:39]
	s_waitcnt lgkmcnt(0)
	s_barrier
	v_and_b32_e32 v57, 15, v0
	v_lshlrev_b32_e32 v57, 2, v57
	ds_read_b32 v57, v57 offset:9216
	s_waitcnt lgkmcnt(0)
	s_nop 1
	v_add_u32_dpp v57, v57, v57 row_shr:1 row_mask:0xf bank_mask:0xf bound_ctrl:0
	s_nop 1
	v_add_u32_dpp v57, v57, v57 row_shr:2 row_mask:0xf bank_mask:0xf bound_ctrl:0
	s_nop 1
	v_add_u32_dpp v57, v57, v57 row_shr:4 row_mask:0xf bank_mask:0xf bound_ctrl:0
	s_nop 1
	v_add_u32_dpp v57, v57, v57 row_shr:8 row_mask:0xf bank_mask:0xf bound_ctrl:0
	s_sub_u32 s15, s3, 1
	s_max_i32 s15, s15, 0
	s_nop 1
	v_readlane_b32 s16, v57, s15
	s_cmp_eq_u32 s3, 0
	s_cselect_b32 s16, 0, s16
	v_sub_u32_e32 v58, v55, v54
	v_add_u32_e32 v58, s16, v58
	v_add_u32_e32 v59, v58, v52
	v_cmp_gt_u32_e32 vcc, 0x224, v0
	s_and_saveexec_b64 s[36:37], vcc
	ds_read_b64 v[56:57], v50
	ds_write_b64 v50, v[58:59] offset:9728
	s_waitcnt lgkmcnt(0)
	v_sub_u32_e32 v56, v56, v58
	v_sub_u32_e32 v57, v57, v59
	ds_write_b64 v50, v[56:57]
	s_mov_b64 exec, s[36:37]
	s_waitcnt lgkmcnt(0)
	s_barrier
	v_mov_b32_e32 v60, 0x447
	v_cmp_gt_i32_e64 s[20:21], 0, v3
	v_subrev_co_u32_e32 v51, vcc, 0x61a80, v3
	v_lshrrev_b32_e32 v51, 6, v51
	v_lshrrev_b32_e32 v52, 9, v3
	v_add_u32_e32 v51, 0x30e, v51
	v_cndmask_b32_e32 v51, v51, v52, vcc
	v_cndmask_b32_e64 v51, v51, v60, s[20:21]
	v_lshlrev_b32_e32 v51, 2, v51
	ds_read_b32 v53, v51 offset:9728
	v_cmp_gt_i32_e64 s[20:21], 0, v5
	v_subrev_co_u32_e32 v51, vcc, 0x61a80, v5
	v_lshrrev_b32_e32 v51, 6, v51
	v_lshrrev_b32_e32 v52, 9, v5
	v_add_u32_e32 v51, 0x30e, v51
	v_cndmask_b32_e32 v51, v51, v52, vcc
	v_cndmask_b32_e64 v51, v51, v60, s[20:21]
	v_lshlrev_b32_e32 v51, 2, v51
	ds_read_b32 v54, v51 offset:9728
	v_cmp_gt_i32_e64 s[20:21], 0, v7
	v_subrev_co_u32_e32 v51, vcc, 0x61a80, v7
	v_lshrrev_b32_e32 v51, 6, v51
	v_lshrrev_b32_e32 v52, 9, v7
	v_add_u32_e32 v51, 0x30e, v51
	v_cndmask_b32_e32 v51, v51, v52, vcc
	v_cndmask_b32_e64 v51, v51, v60, s[20:21]
	v_lshlrev_b32_e32 v51, 2, v51
	ds_read_b32 v55, v51 offset:9728
	v_cmp_gt_i32_e64 s[20:21], 0, v9
	v_subrev_co_u32_e32 v51, vcc, 0x61a80, v9
	v_lshrrev_b32_e32 v51, 6, v51
	v_lshrrev_b32_e32 v52, 9, v9
	v_add_u32_e32 v51, 0x30e, v51
	v_cndmask_b32_e32 v51, v51, v52, vcc
	v_cndmask_b32_e64 v51, v51, v60, s[20:21]
	v_lshlrev_b32_e32 v51, 2, v51
	ds_read_b32 v56, v51 offset:9728
	s_waitcnt lgkmcnt(0)
	v_add_u32_e32 v34, v34, v53
	v_add_u32_e32 v35, v35, v54
	v_add_u32_e32 v36, v36, v55
	v_add_u32_e32 v37, v37, v56
	v_cmp_gt_i32_e64 s[20:21], 0, v11
	v_subrev_co_u32_e32 v51, vcc, 0x61a80, v11
	v_lshrrev_b32_e32 v51, 6, v51
	v_lshrrev_b32_e32 v52, 9, v11
	v_add_u32_e32 v51, 0x30e, v51
	v_cndmask_b32_e32 v51, v51, v52, vcc
	v_cndmask_b32_e64 v51, v51, v60, s[20:21]
	v_lshlrev_b32_e32 v51, 2, v51
	ds_read_b32 v53, v51 offset:9728
	v_cmp_gt_i32_e64 s[20:21], 0, v13
	v_subrev_co_u32_e32 v51, vcc, 0x61a80, v13
	v_lshrrev_b32_e32 v51, 6, v51
	v_lshrrev_b32_e32 v52, 9, v13
	v_add_u32_e32 v51, 0x30e, v51
	v_cndmask_b32_e32 v51, v51, v52, vcc
	v_cndmask_b32_e64 v51, v51, v60, s[20:21]
	v_lshlrev_b32_e32 v51, 2, v51
	ds_read_b32 v54, v51 offset:9728
	v_cmp_gt_i32_e64 s[20:21], 0, v15
	v_subrev_co_u32_e32 v51, vcc, 0x61a80, v15
	v_lshrrev_b32_e32 v51, 6, v51
	v_lshrrev_b32_e32 v52, 9, v15
	v_add_u32_e32 v51, 0x30e, v51
	v_cndmask_b32_e32 v51, v51, v52, vcc
	v_cndmask_b32_e64 v51, v51, v60, s[20:21]
	v_lshlrev_b32_e32 v51, 2, v51
	ds_read_b32 v55, v51 offset:9728
	v_cmp_gt_i32_e64 s[20:21], 0, v17
	v_subrev_co_u32_e32 v51, vcc, 0x61a80, v17
	v_lshrrev_b32_e32 v51, 6, v51
	v_lshrrev_b32_e32 v52, 9, v17
	v_add_u32_e32 v51, 0x30e, v51
	v_cndmask_b32_e32 v51, v51, v52, vcc
	v_cndmask_b32_e64 v51, v51, v60, s[20:21]
	v_lshlrev_b32_e32 v51, 2, v51
	ds_read_b32 v56, v51 offset:9728
	s_waitcnt lgkmcnt(0)
	v_add_u32_e32 v38, v38, v53
	v_add_u32_e32 v39, v39, v54
	v_add_u32_e32 v40, v40, v55
	v_add_u32_e32 v41, v41, v56
	v_cmp_gt_i32_e64 s[20:21], 0, v19
	v_subrev_co_u32_e32 v51, vcc, 0x61a80, v19
	v_lshrrev_b32_e32 v51, 6, v51
	v_lshrrev_b32_e32 v52, 9, v19
	v_add_u32_e32 v51, 0x30e, v51
	v_cndmask_b32_e32 v51, v51, v52, vcc
	v_cndmask_b32_e64 v51, v51, v60, s[20:21]
	v_lshlrev_b32_e32 v51, 2, v51
	ds_read_b32 v53, v51 offset:9728
	v_cmp_gt_i32_e64 s[20:21], 0, v21
	v_subrev_co_u32_e32 v51, vcc, 0x61a80, v21
	v_lshrrev_b32_e32 v51, 6, v51
	v_lshrrev_b32_e32 v52, 9, v21
	v_add_u32_e32 v51, 0x30e, v51
	v_cndmask_b32_e32 v51, v51, v52, vcc
	v_cndmask_b32_e64 v51, v51, v60, s[20:21]
	v_lshlrev_b32_e32 v51, 2, v51
	ds_read_b32 v54, v51 offset:9728
	v_cmp_gt_i32_e64 s[20:21], 0, v23
	v_subrev_co_u32_e32 v51, vcc, 0x61a80, v23
	v_lshrrev_b32_e32 v51, 6, v51
	v_lshrrev_b32_e32 v52, 9, v23
	v_add_u32_e32 v51, 0x30e, v51
	v_cndmask_b32_e32 v51, v51, v52, vcc
	v_cndmask_b32_e64 v51, v51, v60, s[20:21]
	v_lshlrev_b32_e32 v51, 2, v51
	ds_read_b32 v55, v51 offset:9728
	v_cmp_gt_i32_e64 s[20:21], 0, v25
	v_subrev_co_u32_e32 v51, vcc, 0x61a80, v25
	v_lshrrev_b32_e32 v51, 6, v51
	v_lshrrev_b32_e32 v52, 9, v25
	v_add_u32_e32 v51, 0x30e, v51
	v_cndmask_b32_e32 v51, v51, v52, vcc
	v_cndmask_b32_e64 v51, v51, v60, s[20:21]
	v_lshlrev_b32_e32 v51, 2, v51
	ds_read_b32 v56, v51 offset:9728
	s_waitcnt lgkmcnt(0)
	v_add_u32_e32 v42, v42, v53
	v_add_u32_e32 v43, v43, v54
	v_add_u32_e32 v44, v44, v55
	v_add_u32_e32 v45, v45, v56
	v_cmp_gt_i32_e64 s[20:21], 0, v27
	v_subrev_co_u32_e32 v51, vcc, 0x61a80, v27
	v_lshrrev_b32_e32 v51, 6, v51
	v_lshrrev_b32_e32 v52, 9, v27
	v_add_u32_e32 v51, 0x30e, v51
	v_cndmask_b32_e32 v51, v51, v52, vcc
	v_cndmask_b32_e64 v51, v51, v60, s[20:21]
	v_lshlrev_b32_e32 v51, 2, v51
	ds_read_b32 v53, v51 offset:9728
	v_cmp_gt_i32_e64 s[20:21], 0, v29
	v_subrev_co_u32_e32 v51, vcc, 0x61a80, v29
	v_lshrrev_b32_e32 v51, 6, v51
	v_lshrrev_b32_e32 v52, 9, v29
	v_add_u32_e32 v51, 0x30e, v51
	v_cndmask_b32_e32 v51, v51, v52, vcc
	v_cndmask_b32_e64 v51, v51, v60, s[20:21]
	v_lshlrev_b32_e32 v51, 2, v51
	ds_read_b32 v54, v51 offset:9728
	v_cmp_gt_i32_e64 s[20:21], 0, v31
	v_subrev_co_u32_e32 v51, vcc, 0x61a80, v31
	v_lshrrev_b32_e32 v51, 6, v51
	v_lshrrev_b32_e32 v52, 9, v31
	v_add_u32_e32 v51, 0x30e, v51
	v_cndmask_b32_e32 v51, v51, v52, vcc
	v_cndmask_b32_e64 v51, v51, v60, s[20:21]
	v_lshlrev_b32_e32 v51, 2, v51
	ds_read_b32 v55, v51 offset:9728
	v_cmp_gt_i32_e64 s[20:21], 0, v33
	v_subrev_co_u32_e32 v51, vcc, 0x61a80, v33
	v_lshrrev_b32_e32 v51, 6, v51
	v_lshrrev_b32_e32 v52, 9, v33
	v_add_u32_e32 v51, 0x30e, v51
	v_cndmask_b32_e32 v51, v51, v52, vcc
	v_cndmask_b32_e64 v51, v51, v60, s[20:21]
	v_lshlrev_b32_e32 v51, 2, v51
	ds_read_b32 v56, v51 offset:9728
	s_waitcnt lgkmcnt(0)
	v_add_u32_e32 v46, v46, v53
	v_add_u32_e32 v47, v47, v54
	v_add_u32_e32 v48, v48, v55
	v_add_u32_e32 v49, v49, v56
	s_mov_b64 s[38:39], exec
	s_movk_i32 s14, 0x4000
	v_cmp_gt_u32_e32 vcc, s14, v34
	v_lshlrev_b32_e32 v52, 3, v34
	s_and_b64 exec, s[38:39], vcc
	ds_write_b64 v52, v[2:3] offset:14336
	s_mov_b64 exec, s[38:39]
	v_cmp_gt_u32_e32 vcc, s14, v35
	v_lshlrev_b32_e32 v52, 3, v35
	s_and_b64 exec, s[38:39], vcc
	ds_write_b64 v52, v[4:5] offset:14336
	s_mov_b64 exec, s[38:39]
	v_cmp_gt_u32_e32 vcc, s14, v36
	v_lshlrev_b32_e32 v52, 3, v36
	s_and_b64 exec, s[38:39], vcc
	ds_write_b64 v52, v[6:7] offset:14336
	s_mov_b64 exec, s[38:39]
	v_cmp_gt_u32_e32 vcc, s14, v37
	v_lshlrev_b32_e32 v52, 3, v37
	s_and_b64 exec, s[38:39], vcc
	ds_write_b64 v52, v[8:9] offset:14336
	s_mov_b64 exec, s[38:39]
	v_cmp_gt_u32_e32 vcc, s14, v38
	v_lshlrev_b32_e32 v52, 3, v38
	s_and_b64 exec, s[38:39], vcc
	ds_write_b64 v52, v[10:11] offset:14336
	s_mov_b64 exec, s[38:39]
	v_cmp_gt_u32_e32 vcc, s14, v39
	v_lshlrev_b32_e32 v52, 3, v39
	s_and_b64 exec, s[38:39], vcc
	ds_write_b64 v52, v[12:13] offset:14336
	s_mov_b64 exec, s[38:39]
	v_cmp_gt_u32_e32 vcc, s14, v40
	v_lshlrev_b32_e32 v52, 3, v40
	s_and_b64 exec, s[38:39], vcc
	ds_write_b64 v52, v[14:15] offset:14336
	s_mov_b64 exec, s[38:39]
	v_cmp_gt_u32_e32 vcc, s14, v41
	v_lshlrev_b32_e32 v52, 3, v41
	s_and_b64 exec, s[38:39], vcc
	ds_write_b64 v52, v[16:17] offset:14336
	s_mov_b64 exec, s[38:39]
	v_cmp_gt_u32_e32 vcc, s14, v42
	v_lshlrev_b32_e32 v52, 3, v42
	s_and_b64 exec, s[38:39], vcc
	ds_write_b64 v52, v[18:19] offset:14336
	s_mov_b64 exec, s[38:39]
	v_cmp_gt_u32_e32 vcc, s14, v43
	v_lshlrev_b32_e32 v52, 3, v43
	s_and_b64 exec, s[38:39], vcc
	ds_write_b64 v52, v[20:21] offset:14336
	s_mov_b64 exec, s[38:39]
	v_cmp_gt_u32_e32 vcc, s14, v44
	v_lshlrev_b32_e32 v52, 3, v44
	s_and_b64 exec, s[38:39], vcc
	ds_write_b64 v52, v[22:23] offset:14336
	s_mov_b64 exec, s[38:39]
	v_cmp_gt_u32_e32 vcc, s14, v45
	v_lshlrev_b32_e32 v52, 3, v45
	s_and_b64 exec, s[38:39], vcc
	ds_write_b64 v52, v[24:25] offset:14336
	s_mov_b64 exec, s[38:39]
	v_cmp_gt_u32_e32 vcc, s14, v46
	v_lshlrev_b32_e32 v52, 3, v46
	s_and_b64 exec, s[38:39], vcc
	ds_write_b64 v52, v[26:27] offset:14336
	s_mov_b64 exec, s[38:39]
	v_cmp_gt_u32_e32 vcc, s14, v47
	v_lshlrev_b32_e32 v52, 3, v47
	s_and_b64 exec, s[38:39], vcc
	ds_write_b64 v52, v[28:29] offset:14336
	s_mov_b64 exec, s[38:39]
	v_cmp_gt_u32_e32 vcc, s14, v48
	v_lshlrev_b32_e32 v52, 3, v48
	s_and_b64 exec, s[38:39], vcc
	ds_write_b64 v52, v[30:31] offset:14336
	s_mov_b64 exec, s[38:39]
	v_cmp_gt_u32_e32 vcc, s14, v49
	v_lshlrev_b32_e32 v52, 3, v49
	s_and_b64 exec, s[38:39], vcc
	ds_write_b64 v52, v[32:33] offset:14336
	s_mov_b64 exec, s[38:39]
	s_waitcnt lgkmcnt(0)
	s_barrier
	v_mov_b32_e32 v61, v0
	v_lshlrev_b32_e32 v62, 3, v61
	ds_read_b64 v[50:51], v62 offset:14336
	s_waitcnt lgkmcnt(0)
	v_subrev_co_u32_e32 v53, vcc, 0x61a80, v51
	v_lshrrev_b32_e32 v53, 6, v53
	v_lshrrev_b32_e32 v54, 9, v51
	v_add_u32_e32 v53, 0x30e, v53
	v_cndmask_b32_e32 v53, v53, v54, vcc
	v_min_u32_e32 v53, 0x447, v53
	v_lshlrev_b32_e32 v53, 2, v53
	ds_read_b32 v53, v53
	v_cmp_le_i32_e32 vcc, 0, v51
	s_waitcnt lgkmcnt(0)
	v_add_u32_e32 v53, v53, v61
	v_lshlrev_b32_e32 v53, 3, v53
	s_and_b64 exec, s[38:39], vcc
	global_store_dwordx2 v53, v[50:51], s[34:35] sc1
	s_mov_b64 exec, s[38:39]
	v_add_u32_e32 v61, 0x400, v0
	v_lshlrev_b32_e32 v62, 3, v61
	ds_read_b64 v[50:51], v62 offset:14336
	s_waitcnt lgkmcnt(0)
	v_subrev_co_u32_e32 v53, vcc, 0x61a80, v51
	v_lshrrev_b32_e32 v53, 6, v53
	v_lshrrev_b32_e32 v54, 9, v51
	v_add_u32_e32 v53, 0x30e, v53
	v_cndmask_b32_e32 v53, v53, v54, vcc
	v_min_u32_e32 v53, 0x447, v53
	v_lshlrev_b32_e32 v53, 2, v53
	ds_read_b32 v53, v53
	v_cmp_le_i32_e32 vcc, 0, v51
	s_waitcnt lgkmcnt(0)
	v_add_u32_e32 v53, v53, v61
	v_lshlrev_b32_e32 v53, 3, v53
	s_and_b64 exec, s[38:39], vcc
	global_store_dwordx2 v53, v[50:51], s[34:35] sc1
	s_mov_b64 exec, s[38:39]
	v_add_u32_e32 v61, 0x800, v0
	v_lshlrev_b32_e32 v62, 3, v61
	ds_read_b64 v[50:51], v62 offset:14336
	s_waitcnt lgkmcnt(0)
	v_subrev_co_u32_e32 v53, vcc, 0x61a80, v51
	v_lshrrev_b32_e32 v53, 6, v53
	v_lshrrev_b32_e32 v54, 9, v51
	v_add_u32_e32 v53, 0x30e, v53
	v_cndmask_b32_e32 v53, v53, v54, vcc
	v_min_u32_e32 v53, 0x447, v53
	v_lshlrev_b32_e32 v53, 2, v53
	ds_read_b32 v53, v53
	v_cmp_le_i32_e32 vcc, 0, v51
	s_waitcnt lgkmcnt(0)
	v_add_u32_e32 v53, v53, v61
	v_lshlrev_b32_e32 v53, 3, v53
	s_and_b64 exec, s[38:39], vcc
	global_store_dwordx2 v53, v[50:51], s[34:35] sc1
	s_mov_b64 exec, s[38:39]
	v_add_u32_e32 v61, 0xc00, v0
	v_lshlrev_b32_e32 v62, 3, v61
	ds_read_b64 v[50:51], v62 offset:14336
	s_waitcnt lgkmcnt(0)
	v_subrev_co_u32_e32 v53, vcc, 0x61a80, v51
	v_lshrrev_b32_e32 v53, 6, v53
	v_lshrrev_b32_e32 v54, 9, v51
	v_add_u32_e32 v53, 0x30e, v53
	v_cndmask_b32_e32 v53, v53, v54, vcc
	v_min_u32_e32 v53, 0x447, v53
	v_lshlrev_b32_e32 v53, 2, v53
	ds_read_b32 v53, v53
	v_cmp_le_i32_e32 vcc, 0, v51
	s_waitcnt lgkmcnt(0)
	v_add_u32_e32 v53, v53, v61
	v_lshlrev_b32_e32 v53, 3, v53
	s_and_b64 exec, s[38:39], vcc
	global_store_dwordx2 v53, v[50:51], s[34:35] sc1
	s_mov_b64 exec, s[38:39]
	v_add_u32_e32 v61, 0x1000, v0
	v_lshlrev_b32_e32 v62, 3, v61
	ds_read_b64 v[50:51], v62 offset:14336
	s_waitcnt lgkmcnt(0)
	v_subrev_co_u32_e32 v53, vcc, 0x61a80, v51
	v_lshrrev_b32_e32 v53, 6, v53
	v_lshrrev_b32_e32 v54, 9, v51
	v_add_u32_e32 v53, 0x30e, v53
	v_cndmask_b32_e32 v53, v53, v54, vcc
	v_min_u32_e32 v53, 0x447, v53
	v_lshlrev_b32_e32 v53, 2, v53
	ds_read_b32 v53, v53
	v_cmp_le_i32_e32 vcc, 0, v51
	s_waitcnt lgkmcnt(0)
	v_add_u32_e32 v53, v53, v61
	v_lshlrev_b32_e32 v53, 3, v53
	s_and_b64 exec, s[38:39], vcc
	global_store_dwordx2 v53, v[50:51], s[34:35] sc1
	s_mov_b64 exec, s[38:39]
	v_add_u32_e32 v61, 0x1400, v0
	v_lshlrev_b32_e32 v62, 3, v61
	ds_read_b64 v[50:51], v62 offset:14336
	s_waitcnt lgkmcnt(0)
	v_subrev_co_u32_e32 v53, vcc, 0x61a80, v51
	v_lshrrev_b32_e32 v53, 6, v53
	v_lshrrev_b32_e32 v54, 9, v51
	v_add_u32_e32 v53, 0x30e, v53
	v_cndmask_b32_e32 v53, v53, v54, vcc
	v_min_u32_e32 v53, 0x447, v53
	v_lshlrev_b32_e32 v53, 2, v53
	ds_read_b32 v53, v53
	v_cmp_le_i32_e32 vcc, 0, v51
	s_waitcnt lgkmcnt(0)
	v_add_u32_e32 v53, v53, v61
	v_lshlrev_b32_e32 v53, 3, v53
	s_and_b64 exec, s[38:39], vcc
	global_store_dwordx2 v53, v[50:51], s[34:35] sc1
	s_mov_b64 exec, s[38:39]
	v_add_u32_e32 v61, 0x1800, v0
	v_lshlrev_b32_e32 v62, 3, v61
	ds_read_b64 v[50:51], v62 offset:14336
	s_waitcnt lgkmcnt(0)
	v_subrev_co_u32_e32 v53, vcc, 0x61a80, v51
	v_lshrrev_b32_e32 v53, 6, v53
	v_lshrrev_b32_e32 v54, 9, v51
	v_add_u32_e32 v53, 0x30e, v53
	v_cndmask_b32_e32 v53, v53, v54, vcc
	v_min_u32_e32 v53, 0x447, v53
	v_lshlrev_b32_e32 v53, 2, v53
	ds_read_b32 v53, v53
	v_cmp_le_i32_e32 vcc, 0, v51
	s_waitcnt lgkmcnt(0)
	v_add_u32_e32 v53, v53, v61
	v_lshlrev_b32_e32 v53, 3, v53
	s_and_b64 exec, s[38:39], vcc
	global_store_dwordx2 v53, v[50:51], s[34:35] sc1
	s_mov_b64 exec, s[38:39]
	v_add_u32_e32 v61, 0x1c00, v0
	v_lshlrev_b32_e32 v62, 3, v61
	ds_read_b64 v[50:51], v62 offset:14336
	s_waitcnt lgkmcnt(0)
	v_subrev_co_u32_e32 v53, vcc, 0x61a80, v51
	v_lshrrev_b32_e32 v53, 6, v53
	v_lshrrev_b32_e32 v54, 9, v51
	v_add_u32_e32 v53, 0x30e, v53
	v_cndmask_b32_e32 v53, v53, v54, vcc
	v_min_u32_e32 v53, 0x447, v53
	v_lshlrev_b32_e32 v53, 2, v53
	ds_read_b32 v53, v53
	v_cmp_le_i32_e32 vcc, 0, v51
	s_waitcnt lgkmcnt(0)
	v_add_u32_e32 v53, v53, v61
	v_lshlrev_b32_e32 v53, 3, v53
	s_and_b64 exec, s[38:39], vcc
	global_store_dwordx2 v53, v[50:51], s[34:35] sc1
	s_mov_b64 exec, s[38:39]
	v_add_u32_e32 v61, 0x2000, v0
	v_lshlrev_b32_e32 v62, 3, v61
	ds_read_b64 v[50:51], v62 offset:14336
	s_waitcnt lgkmcnt(0)
	v_subrev_co_u32_e32 v53, vcc, 0x61a80, v51
	v_lshrrev_b32_e32 v53, 6, v53
	v_lshrrev_b32_e32 v54, 9, v51
	v_add_u32_e32 v53, 0x30e, v53
	v_cndmask_b32_e32 v53, v53, v54, vcc
	v_min_u32_e32 v53, 0x447, v53
	v_lshlrev_b32_e32 v53, 2, v53
	ds_read_b32 v53, v53
	v_cmp_le_i32_e32 vcc, 0, v51
	s_waitcnt lgkmcnt(0)
	v_add_u32_e32 v53, v53, v61
	v_lshlrev_b32_e32 v53, 3, v53
	s_and_b64 exec, s[38:39], vcc
	global_store_dwordx2 v53, v[50:51], s[34:35] sc1
	s_mov_b64 exec, s[38:39]
	v_add_u32_e32 v61, 0x2400, v0
	v_lshlrev_b32_e32 v62, 3, v61
	ds_read_b64 v[50:51], v62 offset:14336
	s_waitcnt lgkmcnt(0)
	v_subrev_co_u32_e32 v53, vcc, 0x61a80, v51
	v_lshrrev_b32_e32 v53, 6, v53
	v_lshrrev_b32_e32 v54, 9, v51
	v_add_u32_e32 v53, 0x30e, v53
	v_cndmask_b32_e32 v53, v53, v54, vcc
	v_min_u32_e32 v53, 0x447, v53
	v_lshlrev_b32_e32 v53, 2, v53
	ds_read_b32 v53, v53
	v_cmp_le_i32_e32 vcc, 0, v51
	s_waitcnt lgkmcnt(0)
	v_add_u32_e32 v53, v53, v61
	v_lshlrev_b32_e32 v53, 3, v53
	s_and_b64 exec, s[38:39], vcc
	global_store_dwordx2 v53, v[50:51], s[34:35] sc1
	s_mov_b64 exec, s[38:39]
	v_add_u32_e32 v61, 0x2800, v0
	v_lshlrev_b32_e32 v62, 3, v61
	ds_read_b64 v[50:51], v62 offset:14336
	s_waitcnt lgkmcnt(0)
	v_subrev_co_u32_e32 v53, vcc, 0x61a80, v51
	v_lshrrev_b32_e32 v53, 6, v53
	v_lshrrev_b32_e32 v54, 9, v51
	v_add_u32_e32 v53, 0x30e, v53
	v_cndmask_b32_e32 v53, v53, v54, vcc
	v_min_u32_e32 v53, 0x447, v53
	v_lshlrev_b32_e32 v53, 2, v53
	ds_read_b32 v53, v53
	v_cmp_le_i32_e32 vcc, 0, v51
	s_waitcnt lgkmcnt(0)
	v_add_u32_e32 v53, v53, v61
	v_lshlrev_b32_e32 v53, 3, v53
	s_and_b64 exec, s[38:39], vcc
	global_store_dwordx2 v53, v[50:51], s[34:35] sc1
	s_mov_b64 exec, s[38:39]
	v_add_u32_e32 v61, 0x2c00, v0
	v_lshlrev_b32_e32 v62, 3, v61
	ds_read_b64 v[50:51], v62 offset:14336
	s_waitcnt lgkmcnt(0)
	v_subrev_co_u32_e32 v53, vcc, 0x61a80, v51
	v_lshrrev_b32_e32 v53, 6, v53
	v_lshrrev_b32_e32 v54, 9, v51
	v_add_u32_e32 v53, 0x30e, v53
	v_cndmask_b32_e32 v53, v53, v54, vcc
	v_min_u32_e32 v53, 0x447, v53
	v_lshlrev_b32_e32 v53, 2, v53
	ds_read_b32 v53, v53
	v_cmp_le_i32_e32 vcc, 0, v51
	s_waitcnt lgkmcnt(0)
	v_add_u32_e32 v53, v53, v61
	v_lshlrev_b32_e32 v53, 3, v53
	s_and_b64 exec, s[38:39], vcc
	global_store_dwordx2 v53, v[50:51], s[34:35] sc1
	s_mov_b64 exec, s[38:39]
	v_add_u32_e32 v61, 0x3000, v0
	v_lshlrev_b32_e32 v62, 3, v61
	ds_read_b64 v[50:51], v62 offset:14336
	s_waitcnt lgkmcnt(0)
	v_subrev_co_u32_e32 v53, vcc, 0x61a80, v51
	v_lshrrev_b32_e32 v53, 6, v53
	v_lshrrev_b32_e32 v54, 9, v51
	v_add_u32_e32 v53, 0x30e, v53
	v_cndmask_b32_e32 v53, v53, v54, vcc
	v_min_u32_e32 v53, 0x447, v53
	v_lshlrev_b32_e32 v53, 2, v53
	ds_read_b32 v53, v53
	v_cmp_le_i32_e32 vcc, 0, v51
	s_waitcnt lgkmcnt(0)
	v_add_u32_e32 v53, v53, v61
	v_lshlrev_b32_e32 v53, 3, v53
	s_and_b64 exec, s[38:39], vcc
	global_store_dwordx2 v53, v[50:51], s[34:35] sc1
	s_mov_b64 exec, s[38:39]
	v_add_u32_e32 v61, 0x3400, v0
	v_lshlrev_b32_e32 v62, 3, v61
	ds_read_b64 v[50:51], v62 offset:14336
	s_waitcnt lgkmcnt(0)
	v_subrev_co_u32_e32 v53, vcc, 0x61a80, v51
	v_lshrrev_b32_e32 v53, 6, v53
	v_lshrrev_b32_e32 v54, 9, v51
	v_add_u32_e32 v53, 0x30e, v53
	v_cndmask_b32_e32 v53, v53, v54, vcc
	v_min_u32_e32 v53, 0x447, v53
	v_lshlrev_b32_e32 v53, 2, v53
	ds_read_b32 v53, v53
	v_cmp_le_i32_e32 vcc, 0, v51
	s_waitcnt lgkmcnt(0)
	v_add_u32_e32 v53, v53, v61
	v_lshlrev_b32_e32 v53, 3, v53
	s_and_b64 exec, s[38:39], vcc
	global_store_dwordx2 v53, v[50:51], s[34:35] sc1
	s_mov_b64 exec, s[38:39]
	v_add_u32_e32 v61, 0x3800, v0
	v_lshlrev_b32_e32 v62, 3, v61
	ds_read_b64 v[50:51], v62 offset:14336
	s_waitcnt lgkmcnt(0)
	v_subrev_co_u32_e32 v53, vcc, 0x61a80, v51
	v_lshrrev_b32_e32 v53, 6, v53
	v_lshrrev_b32_e32 v54, 9, v51
	v_add_u32_e32 v53, 0x30e, v53
	v_cndmask_b32_e32 v53, v53, v54, vcc
	v_min_u32_e32 v53, 0x447, v53
	v_lshlrev_b32_e32 v53, 2, v53
	ds_read_b32 v53, v53
	v_cmp_le_i32_e32 vcc, 0, v51
	s_waitcnt lgkmcnt(0)
	v_add_u32_e32 v53, v53, v61
	v_lshlrev_b32_e32 v53, 3, v53
	s_and_b64 exec, s[38:39], vcc
	global_store_dwordx2 v53, v[50:51], s[34:35] sc1
	s_mov_b64 exec, s[38:39]
	v_add_u32_e32 v61, 0x3c00, v0
	v_lshlrev_b32_e32 v62, 3, v61
	ds_read_b64 v[50:51], v62 offset:14336
	s_waitcnt lgkmcnt(0)
	v_subrev_co_u32_e32 v53, vcc, 0x61a80, v51
	v_lshrrev_b32_e32 v53, 6, v53
	v_lshrrev_b32_e32 v54, 9, v51
	v_add_u32_e32 v53, 0x30e, v53
	v_cndmask_b32_e32 v53, v53, v54, vcc
	v_min_u32_e32 v53, 0x447, v53
	v_lshlrev_b32_e32 v53, 2, v53
	ds_read_b32 v53, v53
	v_cmp_le_i32_e32 vcc, 0, v51
	s_waitcnt lgkmcnt(0)
	v_add_u32_e32 v53, v53, v61
	v_lshlrev_b32_e32 v53, 3, v53
	s_and_b64 exec, s[38:39], vcc
	global_store_dwordx2 v53, v[50:51], s[34:35] sc1
	s_mov_b64 exec, s[38:39]
	s_endpgm
